# phase 4 HGRN pass-3 work queue: the next unit index is fetched (returning atomic into a spare VGPR) while the current unit runs, instead of one round trip plus two barriers of idle time per unit
# baseline (speedup 1.0000x reference)
; #define LAS __attribute__((address_space(3)))
; __device__ __forceinline__ unsigned cvt_pk_bf16(float lo, float hi) { unsigned r; asm volatile("v_cvt_pk_bf16_f32 %0, %1, %2" : "=v"(r) : "v"(lo), "v"(hi)); return r; }
; __device__ __forceinline__ void hg3_unit(Frame& F, int l, int unit) {
;     ...
;     const int r32 = F.lane & 31, hi = F.lane >> 5;
;     if (F.wave < 3) {
;         const int tb = F.wave == 0 ? 0 : 1, sb = F.wave == 2 ? 1 : 0; const int kbase = (F.wave == 1) ? HG_KB : (HG_KA + sb * 32 * HP128);
;         f32x16 acc = {};
; #pragma unroll
;         for (int ks = 0; ks < 8; ++ks) { const bf16x8 a = *(const LAS bf16x8*)(F.lds + HG_QA + (32 * tb + r32) * HP128 + ks * 32 + hi * 16);
;             const bf16x8 bb = *(const LAS bf16x8*)(F.lds + kbase + r32 * HP128 + ks * 32 + hi * 16);
;             acc = __builtin_amdgcn_mfma_f32_32x32x16_bf16(a, bb, acc, 0, 0, 0); }
; #pragma unroll
;         for (int r = 0; r < 16; ++r) { const int tl = (r & 3) + 8 * (r >> 2) + 4 * hi;
;             float v = acc[r]; if (F.wave != 1 && r32 > tl) v = 0.f;
;             *(LAS bf16_t*)(F.lds + HG_P + (32 * tb + tl) * HP64 + (32 * sb + r32) * 2) = (bf16_t)(cvt_pk_bf16(v, 0.f) & 0xffffu); }
;     } else if (F.wave == 3) {
; #pragma unroll
;         for (int r = 0; r < 16; ++r) { const int tl = (r & 3) + 8 * (r >> 2) + 4 * hi; *(LAS bf16_t*)(F.lds + HG_P + tl * HP64 + (32 + r32) * 2) = 0; }
;     }
.LBB0_973:
	s_lshl_b32 s34, s80, 6
	s_lshl_b64 s[4:5], s[34:35], 2
	s_add_u32 s4, s48, s4
	s_addc_u32 s5, s49, s5
	s_add_u32 s44, s4, 0x80000
	s_addc_u32 s45, s5, 0
	s_lshl_b32 s34, s80, 9
	s_lshl_b64 s[4:5], s[34:35], 2
	s_add_u32 s4, s94, s4
	s_addc_u32 s5, s95, s5
	s_add_u32 s46, s4, 0x205c0000
	v_ashrrev_i32_e32 v9, 5, v205
	s_addc_u32 s47, s5, 0
	v_and_b32_e32 v8, 31, v205
	v_lshlrev_b32_e32 v10, 2, v9
	v_readlane_b32 s10, v250, 4
	s_add_u32 s6, s94, 0x225c1000
	v_cmp_gt_i32_e32 vcc, v8, v10
	v_readlane_b32 s11, v250, 5
	v_or_b32_e32 v15, 1, v10
	s_addc_u32 s7, s95, 0
	s_and_b64 s[52:53], s[10:11], vcc
	v_cmp_gt_i32_e32 vcc, v8, v15
	v_or_b32_e32 v16, 2, v10
	s_and_b64 s[66:67], s[10:11], vcc
	v_cmp_gt_i32_e32 vcc, v8, v16
	v_or_b32_e32 v17, 3, v10
	s_and_b64 s[68:69], s[10:11], vcc
	v_cmp_gt_i32_e32 vcc, v8, v17
	v_add_u32_e32 v18, 8, v10
	s_and_b64 s[70:71], s[10:11], vcc
	v_cmp_gt_i32_e32 vcc, v8, v18
	v_add_u32_e32 v19, 9, v10
	s_and_b64 s[72:73], s[10:11], vcc
	v_cmp_gt_i32_e32 vcc, v8, v19
	v_add_u32_e32 v20, 10, v10
	s_and_b64 s[74:75], s[10:11], vcc
	v_cmp_gt_i32_e32 vcc, v8, v20
	v_add_u32_e32 v21, 11, v10
	v_lshlrev_b32_e32 v5, 4, v204
	s_and_b64 s[76:77], s[10:11], vcc
	v_cmp_gt_i32_e32 vcc, v8, v21
	v_add_u32_e32 v22, 16, v10
	v_and_b32_e32 v0, 0xf0, v5
	s_and_b64 s[64:65], s[10:11], vcc
	v_cmp_gt_i32_e32 vcc, v8, v22
	v_add_u32_e32 v23, 17, v10
	v_lshl_add_u64 v[2:3], s[94:95], 0, v[0:1]
	s_mov_b64 s[4:5], 0x2ce81000
	s_and_b64 s[50:51], s[10:11], vcc
	v_cmp_gt_i32_e32 vcc, v8, v23
	v_add_u32_e32 v24, 18, v10
	v_lshl_add_u64 v[26:27], v[2:3], 0, s[4:5]
	v_lshlrev_b32_e32 v62, 2, v205
	v_readlane_b32 s4, v249, 55
	s_and_b64 s[36:37], s[10:11], vcc
	v_cmp_gt_i32_e32 vcc, v8, v24
	v_add_u32_e32 v25, 19, v10
	v_add_u32_e32 v36, s4, v62
	s_movk_i32 s4, 0x120
	v_readlane_b32 s9, v250, 8
	s_and_b64 s[62:63], s[10:11], vcc
	v_cmp_gt_i32_e32 vcc, v8, v25
	v_add_u32_e32 v38, 24, v10
	v_mul_lo_u32 v2, v205, s4
	s_movk_i32 s4, 0x240
	s_movk_i32 s12, 0x90
	s_and_b64 s[48:49], s[10:11], vcc
	v_cmp_gt_i32_e32 vcc, v8, v38
	v_add_u32_e32 v38, s9, v38
	v_lshlrev_b32_e32 v11, 1, v8
	v_mul_lo_u32 v12, v9, s4
	v_readlane_b32 s4, v250, 9
	v_readlane_b32 s15, v249, 61
	v_mul_lo_u32 v38, v38, s12
	v_add3_u32 v11, 0, v11, v12
	v_mov_b32_e32 v12, s4
	v_readlane_b32 s4, v250, 3
	v_add_u32_e32 v42, s15, v38
	v_add_u32_e32 v38, 25, v10
	v_or_b32_e32 v13, s4, v8
	s_and_b64 s[4:5], s[10:11], vcc
	v_cmp_gt_i32_e32 vcc, v8, v38
	v_add_u32_e32 v38, s9, v38
	v_mul_lo_u32 v38, v38, s12
	v_add_u32_e32 v43, s15, v38
	v_add_u32_e32 v38, 26, v10
	s_and_b64 s[86:87], s[10:11], vcc
	v_cmp_gt_i32_e32 vcc, v8, v38
	v_add_u32_e32 v38, s9, v38
	v_mul_lo_u32 v38, v38, s12
	v_add_u32_e32 v44, s15, v38
	v_add_u32_e32 v38, 27, v10
	s_and_b64 s[60:61], s[10:11], vcc
	v_cmp_gt_i32_e32 vcc, v8, v38
	v_add_u32_e32 v38, s9, v38
	s_and_b64 s[40:41], s[10:11], vcc
	v_mul_lo_u32 v38, v38, s12
	v_readlane_b32 s10, v250, 11
	v_lshlrev_b32_e32 v4, 3, v204
	s_movk_i32 s13, 0x110
	v_add_u32_e32 v45, s15, v38
	v_or_b32_e32 v38, s10, v8
	v_and_b32_e32 v28, 0xffffff80, v4
	s_add_i32 s8, 0, 0x15a00
	v_add_u32_e32 v4, 0x200, v204
	v_add_u32_e32 v6, 0x400, v204
	v_add_u32_e32 v7, 0x600, v204
	v_add_u32_e32 v64, 0x13640, v11
	v_add_u32_e32 v65, 0x136d0, v11
	v_add_u32_e32 v66, 0x13760, v11
	v_add_u32_e32 v67, 0x137f0, v11
	v_add_u32_e32 v68, 0x13ac0, v11
	v_add_u32_e32 v69, 0x13b50, v11
	v_add_u32_e32 v70, 0x13be0, v11
	v_add_u32_e32 v71, 0x13c70, v11
	v_add_u32_e32 v72, 0x13f40, v11
	v_add_u32_e32 v73, 0x13fd0, v11
	v_add_u32_e32 v74, 0x14060, v11
	v_add_u32_e32 v75, 0x140f0, v11
; #define LAS __attribute__((address_space(3)))
; #define LDS_WAIT() asm volatile("s_waitcnt lgkmcnt(0)" ::: "memory")
; __device__ __forceinline__ void hg3_unit(Frame& F, int l, int unit) {
;     ...
;     const int r32 = F.lane & 31, hi = F.lane >> 5;
;     if (F.wave < 3) {
;         const int tb = F.wave == 0 ? 0 : 1, sb = F.wave == 2 ? 1 : 0; const int kbase = (F.wave == 1) ? HG_KB : (HG_KA + sb * 32 * HP128);
;         f32x16 acc = {};
; #pragma unroll
;         for (int ks = 0; ks < 8; ++ks) { const bf16x8 a = *(const LAS bf16x8*)(F.lds + HG_QA + (32 * tb + r32) * HP128 + ks * 32 + hi * 16);
;             const bf16x8 bb = *(const LAS bf16x8*)(F.lds + kbase + r32 * HP128 + ks * 32 + hi * 16);
;             acc = __builtin_amdgcn_mfma_f32_32x32x16_bf16(a, bb, acc, 0, 0, 0); }
; #pragma unroll
;         for (int r = 0; r < 16; ++r) { const int tl = (r & 3) + 8 * (r >> 2) + 4 * hi;
;             float v = acc[r]; if (F.wave != 1 && r32 > tl) v = 0.f;
;             *(LAS bf16_t*)(F.lds + HG_P + (32 * tb + tl) * HP64 + (32 * sb + r32) * 2) = (bf16_t)(cvt_pk_bf16(v, 0.f) & 0xffffu); }
;     } else if (F.wave == 3) {
; #pragma unroll
;         for (int r = 0; r < 16; ++r) { const int tl = (r & 3) + 8 * (r >> 2) + 4 * hi; *(LAS bf16_t*)(F.lds + HG_P + tl * HP64 + (32 + r32) * 2) = 0; }
;     }
;     LDS_WAIT(); __syncthreads();
;     f32x16 o = {};
;     { const int tb = F.wave >> 2, vb = F.wave & 3;
; #pragma unroll
;       for (int ks = 0; ks < 4; ++ks) { const bf16x8 a = *(const LAS bf16x8*)(F.lds + HG_P + (32 * tb + r32) * HP64 + ks * 32 + hi * 16);
;           const bf16x8 bb = *(const LAS bf16x8*)(F.lds + HG_IT + (32 * vb + r32) * HP64 + ks * 32 + hi * 16);
;           o = __builtin_amdgcn_mfma_f32_32x32x16_bf16(a, bb, o, 0, 0, 0); }
; #pragma unroll
;       for (int ks = 0; ks < 8; ++ks) { const bf16x8 a = *(const LAS bf16x8*)(F.lds + HG_QH + (32 * tb + r32) * HP128 + ks * 32 + hi * 16);
;           const bf16x8 bb = *(const LAS bf16x8*)(F.lds + HG_SPT + (32 * vb + r32) * HP128 + ks * 32 + hi * 16);
;           o = __builtin_amdgcn_mfma_f32_32x32x16_bf16(a, bb, o, 0, 0, 0); }
;       LDS_WAIT(); __syncthreads();
;       LAS float* O = (LAS float*)(F.lds);
; #pragma unroll
;       for (int r = 0; r < 16; ++r) { const int t = 32 * tb + (r & 3) + 8 * (r >> 2) + 4 * hi; O[t * 132 + 32 * vb + r32] = o[r]; }
;     }
;     LDS_WAIT(); __syncthreads();
	v_add_u32_e32 v76, 0x143c0, v11
	v_add_u32_e32 v77, 0x14450, v11
	v_add_u32_e32 v78, 0x144e0, v11
	v_add_u32_e32 v79, 0x14570, v11
	v_or_b32_e32 v11, s9, v8
	v_add_u32_e32 v14, s9, v10
	v_add_u32_e32 v15, s9, v15
	v_add_u32_e32 v16, s9, v16
	v_add_u32_e32 v17, s9, v17
	v_add_u32_e32 v18, s9, v18
	v_add_u32_e32 v19, s9, v19
	v_add_u32_e32 v20, s9, v20
	v_add_u32_e32 v21, s9, v21
	v_add_u32_e32 v22, s9, v22
	v_add_u32_e32 v23, s9, v23
	v_add_u32_e32 v24, s9, v24
	v_add_u32_e32 v25, s9, v25
	v_mul_lo_u32 v40, v38, s12
	v_readlane_b32 s9, v250, 12
	v_mul_lo_u32 v38, v38, s13
	v_lshrrev_b32_e32 v3, 4, v204
	v_lshrrev_b32_e32 v4, 4, v4
	v_lshrrev_b32_e32 v6, 4, v6
	v_lshrrev_b32_e32 v7, 4, v7
	v_add_u32_e32 v46, s15, v40
	v_or_b32_e32 v40, s9, v8
	v_add_u32_e32 v48, 0, v38
	v_mov_b32_e32 v38, s8
	v_mul_lo_u32 v3, v3, s13
	v_mul_lo_u32 v4, v4, s13
	v_mul_lo_u32 v6, v6, s13
	v_mul_lo_u32 v7, v7, s13
	v_mad_u32_u24 v49, v40, s13, v38
	v_ashrrev_i32_e32 v80, 3, v204
	v_and_b32_e32 v38, 0x70, v5
	s_movk_i32 s11, 0x210
	v_add_u32_e32 v3, s8, v3
	v_add_u32_e32 v4, s8, v4
	v_add_u32_e32 v6, s8, v6
	v_add_u32_e32 v7, s8, v7
	v_mad_u32_u24 v47, v40, s12, 0
	v_readlane_b32 s8, v250, 22
	v_mul_lo_u32 v5, v80, s11
	v_lshlrev_b32_e32 v40, 2, v38
	v_mad_u32_u24 v12, v8, s13, v12
	v_mul_lo_u32 v14, v14, s12
	v_mul_lo_u32 v15, v15, s12
	v_mul_lo_u32 v16, v16, s12
	v_mul_lo_u32 v17, v17, s12
	v_mul_lo_u32 v18, v18, s12
	v_mul_lo_u32 v19, v19, s12
	v_mul_lo_u32 v20, v20, s12
	v_mul_lo_u32 v21, v21, s12
	v_mul_lo_u32 v22, v22, s12
	v_mul_lo_u32 v23, v23, s12
	v_mul_lo_u32 v24, v24, s12
	v_mul_lo_u32 v25, v25, s12
	v_lshl_add_u32 v8, v8, 2, s8
	v_add3_u32 v81, 0, v5, v40
	v_mad_i64_i32 v[40:41], s[8:9], v80, s14, 0
	v_add_u32_e32 v5, s10, v10
	v_add_u32_e32 v30, 0x1000, v28
	v_add_u32_e32 v32, 0x2000, v28
	v_add_u32_e32 v34, 0x3000, v28
	v_mad_u32_u24 v11, v11, s13, 0
	v_lshlrev_b32_e32 v9, 4, v9
	v_lshlrev_b32_e32 v13, 1, v13
	v_add_u32_e32 v14, s15, v14
	v_add_u32_e32 v15, s15, v15
	v_add_u32_e32 v16, s15, v16
	v_add_u32_e32 v17, s15, v17
	v_add_u32_e32 v18, s15, v18
	v_add_u32_e32 v19, s15, v19
	v_add_u32_e32 v20, s15, v20
	v_add_u32_e32 v21, s15, v21
	v_add_u32_e32 v22, s15, v22
	v_add_u32_e32 v23, s15, v23
	v_add_u32_e32 v24, s15, v24
	v_add_u32_e32 v25, s15, v25
	s_mov_b32 s31, s35
	s_add_u32 s38, s94, 0x28dc1000
	v_mul_lo_u32 v5, v5, s11
	v_readlane_b32 s8, v252, 62
	v_cmp_eq_u32_e64 s[56:57], 0, v204
	v_lshlrev_b32_e32 v39, 1, v205
	v_ashrrev_i32_e32 v29, 31, v28
	v_ashrrev_i32_e32 v31, 31, v30
	v_ashrrev_i32_e32 v33, 31, v32
	v_ashrrev_i32_e32 v35, 31, v34
	v_mov_b32_e32 v37, v1
	v_lshlrev_b32_e32 v63, 3, v205
	s_addc_u32 s39, s95, 0
	v_add_u32_e32 v82, s8, v2
	v_add_u32_e32 v83, v3, v0
	v_add_u32_e32 v84, v4, v0
	v_add_u32_e32 v85, v6, v0
	v_add_u32_e32 v86, v7, v0
	v_add_u32_e32 v87, v11, v9
	v_add_u32_e32 v88, v12, v9
	v_add_u32_e32 v89, v14, v13
	v_add_u32_e32 v90, v15, v13
	v_add_u32_e32 v91, v16, v13
	v_add_u32_e32 v92, v17, v13
	v_add_u32_e32 v93, v18, v13
	v_add_u32_e32 v94, v19, v13
	v_add_u32_e32 v95, v20, v13
	v_add_u32_e32 v96, v21, v13
	v_add_u32_e32 v97, v22, v13
	v_add_u32_e32 v98, v23, v13
	v_add_u32_e32 v99, v24, v13
	v_add_u32_e32 v100, v25, v13
	v_add_u32_e32 v101, v42, v13
	v_add_u32_e32 v102, v43, v13
	v_add_u32_e32 v103, v44, v13
	v_add_u32_e32 v104, v45, v13
	v_add_u32_e32 v105, v46, v9
	v_add_u32_e32 v106, v47, v9
	v_add_u32_e32 v107, v48, v9
	v_add_u32_e32 v108, v49, v9
	v_add_u32_e32 v109, v8, v5
	s_lshl_b64 s[80:81], s[30:31], 2
	v_writelane_b32 v248, s83, 36
	s_barrier
	s_mov_b32 s100, 0
	s_branch .LBB0_976

; #define LDS_WAIT() asm volatile("s_waitcnt lgkmcnt(0)" ::: "memory")
; __global__ void __launch_bounds__(NTHR, 2) mega_fwd(Args args) {
;     ...
;             for (;;) {
;                 __syncthreads();
;                 if (F.tid == 0) F.MISC[16] = __hip_atomic_fetch_add(F.ctl + CW_HQ + l * 64, 1u, RLX_AGENT);
;                 LDS_WAIT(); __syncthreads();
;                 const int u = (int)F.MISC[16]; if (u >= 512) break;
.LBB0_976:
	s_barrier
	s_and_saveexec_b64 s[58:59], s[56:57]
	s_cbranch_execz .LBB0_980
	s_mov_b64 s[82:83], exec
	v_mbcnt_lo_u32_b32 v0, s82, 0
	v_mbcnt_hi_u32_b32 v0, s83, v0
	v_cmp_eq_u32_e32 vcc, 0, v0
	s_and_saveexec_b64 s[94:95], vcc
	s_cbranch_execz .LBB0_979
	s_bcnt1_i32_b64 s8, s[82:83]
	v_mov_b32_e32 v2, s8
	s_cmp_lg_u32 s100, 0
	s_cbranch_scc1 .Lhq_have
	global_atomic_add v254, v1, v2, s[44:45] sc0
	s_mov_b32 s100, 1
.Lhq_have:
	s_waitcnt vmcnt(0)
	v_mov_b32_e32 v255, v254
	s_nop 1
	global_atomic_add v254, v1, v2, s[44:45] sc0
	v_mov_b32_e32 v2, v255
.LBB0_979:
	s_or_b64 exec, exec, s[94:95]
	s_waitcnt vmcnt(1)
	v_readfirstlane_b32 s8, v2
	s_nop 1
	v_add_u32_e32 v0, s8, v0
	v_readlane_b32 s8, v249, 62
	s_nop 1
	v_mov_b32_e32 v2, s8
	ds_write_b32 v2, v0
